# t1_identity
# speedup vs baseline: 1.1125x; 1.1125x over previous
_Z11align_fusedPKfS0_PKiPf:
	s_load_dwordx2 s[6:7], s[0:1], 0x0
	s_mul_hi_u32 s3, s2, 0x1770
	s_mulk_i32 s2, 0x1770
	s_lshl_b64 s[4:5], s[2:3], 2
	s_waitcnt lgkmcnt(0)
	s_add_u32 s2, s6, s4
	s_addc_u32 s3, s7, s5
	v_mov_b32_e32 v31, 0
	v_lshlrev_b32_e32 v30, 4, v0
	v_lshl_add_u64 v[10:11], s[2:3], 0, v[30:31]
	s_movk_i32 s7, 0x2000
	v_add_co_u32_e32 v12, vcc, s7, v10
	s_movk_i32 s7, 0x3000
	s_nop 0
	v_addc_co_u32_e32 v13, vcc, 0, v11, vcc
	v_add_co_u32_e32 v18, vcc, s7, v10
	s_movk_i32 s6, 0xdc
	s_nop 0
	v_addc_co_u32_e32 v19, vcc, 0, v11, vcc
	v_add_co_u32_e32 v20, vcc, 0x4000, v10
	v_or_b32_e32 v48, 0x400, v0
	s_nop 0
	v_addc_co_u32_e32 v21, vcc, 0, v11, vcc
	v_or_b32_e32 v1, 0x500, v0
	v_cmp_gt_u32_e32 vcc, s6, v0
	global_load_dwordx4 v[2:5], v[12:13], off offset:-4096 nt
	global_load_dwordx4 v[6:9], v[12:13], off nt
	v_cndmask_b32_e32 v1, v48, v1, vcc
	global_load_dwordx4 v[10:13], v[18:19], off nt
	global_load_dwordx4 v[14:17], v[20:21], off nt
	v_lshlrev_b32_e32 v49, 4, v1
	global_load_dwordx4 v[22:25], v30, s[2:3] nt
	global_load_dwordx4 v[18:21], v49, s[2:3] nt
	v_and_b32_e32 v29, 63, v0
	v_cmp_gt_u32_e32 vcc, 64, v0
	v_mov_b32_e32 v26, v31
	v_mov_b32_e32 v27, v31
	v_mov_b32_e32 v28, v31
	s_and_saveexec_b64 s[2:3], vcc
	s_cbranch_execz .LBB0_2
	s_load_dwordx4 s[8:11], s[0:1], 0x8
	v_mul_u32_u24_e32 v1, 3, v29
	v_lshlrev_b32_e32 v31, 2, v29
	v_lshlrev_b32_e32 v1, 2, v1
	s_waitcnt lgkmcnt(0)
	global_load_dword v32, v31, s[10:11]
	global_load_dwordx3 v[26:28], v1, s[8:9] nt
	s_waitcnt vmcnt(1)
	v_lshl_add_u32 v31, v32, 1, v32
